# baseline (speedup 1.0000x reference)
_Z15gemm_qkv_kernelPKDF16_S0_PDF16_S1_S1_PKfS3_S3_S3_S3_S1_PKiPyPj:
	s_load_dwordx8 s[36:43], s[0:1], 0x40
	s_load_dwordx4 s[28:31], s[0:1], 0x60
	s_mov_b64 s[4:5], -1
	s_cmpk_lt_i32 s2, 0x40
	s_movk_i32 s3, 0xc0
	s_cbranch_scc1 .LBB1_30
	s_add_i32 s2, s2, 0xffffffc0
	v_lshlrev_b32_e32 v1, 4, v0
	v_and_b32_e32 v2, 32, v0
	v_lshrrev_b32_e32 v4, 1, v0
	v_lshrrev_b32_e32 v5, 5, v0
	v_or_b32_e32 v13, 0x2000, v1
	s_load_dwordx16 s[12:27], s[0:1], 0x0
	v_bfe_u32 v12, v0, 2, 4
	v_bitop3_b32 v10, v1, v2, 48 bitop3:0x6c
	v_and_b32_e32 v4, 24, v4
	v_and_b32_e32 v5, 4, v5
	v_bfe_u32 v6, v0, 2, 2
	v_lshrrev_b32_e32 v1, 7, v13
	s_movk_i32 s0, 0x70
	s_ashr_i32 s33, s2, 31
	v_lshrrev_b32_e32 v3, 2, v0
	v_and_b32_e32 v11, 64, v0
	v_or3_b32 v4, v5, v6, v4
	v_and_or_b32 v1, v1, s0, v12
	s_lshr_b32 s0, s33, 29
	v_readfirstlane_b32 s1, v0
	v_or_b32_e32 v2, v10, v11
	v_and_or_b32 v3, v3, 64, v4
	s_add_i32 s0, s2, s0
	s_lshr_b32 s10, s1, 6
	v_lshl_or_b32 v164, v3, 12, v2
	v_lshrrev_b32_e32 v3, 6, v13
	s_ashr_i32 s4, s0, 3
	s_and_b32 s0, s0, -8
	v_and_or_b32 v3, v3, s3, v4
	s_lshr_b32 s44, s1, 8
	s_lshl_b32 s3, s10, 10
	s_sub_i32 s0, s2, s0
	s_cmp_lt_i32 s0, 0
	s_cselect_b32 s5, 25, 24
	s_mul_i32 s0, s0, s5
	s_add_i32 s0, s0, s4
	s_mul_hi_i32 s4, s0, 0x2aaaaaab
	s_lshr_b32 s5, s4, 31
	s_ashr_i32 s4, s4, 4
	s_add_i32 s4, s4, s5
	s_lshl_b32 s5, s4, 3
	s_mulk_i32 s4, 0x60
	s_sub_i32 s4, s0, s4
	s_bfe_i32 s0, s4, 0x80000
	s_bfe_u32 s0, s0, 0x3000c
	s_add_i32 s6, s4, s0
	s_bfe_i32 s0, s6, 0x80000
	s_and_b32 s6, s6, 0xf8
	s_sub_i32 s4, s4, s6
	s_sext_i32_i16 s0, s0
	s_sext_i32_i8 s4, s4
	s_lshr_b32 s0, s0, 3
	s_add_i32 s4, s5, s4
	s_ashr_i32 s5, s4, 31
	s_bfe_i64 s[8:9], s[0:1], 0x100000
	s_lshl_b64 s[6:7], s[4:5], 20
	s_lshl_b64 s[8:9], s[8:9], 20
	s_waitcnt lgkmcnt(0)
	s_mov_b32 s94, 0
	s_add_u32 s80, s20, 0x408000
	s_addc_u32 s81, s21, 0
	v_and_b32_e32 v241, 63, v0
	v_lshlrev_b32_e32 v241, 2, v241
	s_add_u32 s8, s14, s8
	s_addc_u32 s9, s15, s9
	s_add_i32 s58, s3, 0
	s_add_i32 m0, s58, 0x10000
	v_lshl_or_b32 v168, v3, 12, v2
	global_load_lds_dwordx4 v164, s[8:9]
	s_add_i32 m0, s58, 0x12000
	s_add_u32 s34, s8, 0x20000
	global_load_lds_dwordx4 v168, s[8:9]
	s_addc_u32 s35, s9, 0
	s_add_i32 m0, s58, 0x14000
	v_lshrrev_b32_e32 v5, 3, v0
	global_load_lds_dwordx4 v164, s[34:35]
	s_add_i32 m0, s58, 0x16000
	s_add_u32 s6, s12, s6
	v_and_or_b32 v5, v5, 48, v12
	s_addc_u32 s7, s13, s7
	s_add_i32 s59, s58, 0x2000
	v_lshl_or_b32 v162, v5, 12, v2
	global_load_lds_dwordx4 v168, s[34:35]
	s_mov_b32 m0, s58
	s_add_u32 s34, s6, 0x80000
	v_lshl_or_b32 v166, v1, 12, v2
	global_load_lds_dwordx4 v162, s[6:7]
	s_mov_b32 m0, s59
	s_addc_u32 s35, s7, 0
	s_add_i32 s60, s58, 0x4000
	global_load_lds_dwordx4 v166, s[6:7]
	s_mov_b32 m0, s60
	s_add_i32 s61, s58, 0x6000
	global_load_lds_dwordx4 v162, s[34:35]
	s_mov_b32 m0, s61
	v_mov_b32_e32 v171, 0
	global_load_lds_dwordx4 v166, s[34:35]
	v_mov_b32_e32 v165, v171
	v_mov_b32_e32 v169, v171
	v_mov_b32_e32 v163, v171
	v_mov_b32_e32 v167, v171
	s_cmp_eq_u32 s44, 1
	s_mov_b32 s11, 0
	v_lshl_add_u64 v[8:9], s[8:9], 0, v[164:165]
	v_lshl_add_u64 v[6:7], s[8:9], 0, v[168:169]
	v_lshl_add_u64 v[2:3], s[6:7], 0, v[162:163]
	s_cselect_b64 s[34:35], -1, 0
	s_cmp_lg_u32 s44, 1
	v_lshl_add_u64 v[4:5], s[6:7], 0, v[166:167]
	s_cbranch_scc1 .LBB1_3
	s_barrier

.LBB1_25:
	s_waitcnt lgkmcnt(0)
	v_add_f32_e32 v170, v170, v205
	v_fmamk_f32 v170, v170, 0x3c800000, v195
	v_mul_f32_e32 v185, 0x4f800000, v170
	v_cmp_gt_f32_e32 vcc, s70, v170
	s_lshl_b32 s10, s8, 1
	s_nop 0
	v_cndmask_b32_e32 v170, v170, v185, vcc
	v_sqrt_f32_e32 v185, v170
	s_nop 0
	v_add_u32_e32 v204, -1, v185
	v_fma_f32 v206, -v204, v185, v170
	v_add_u32_e32 v205, 1, v185
	v_cmp_ge_f32_e64 s[4:5], 0, v206
	s_nop 1
	v_cndmask_b32_e64 v204, v185, v204, s[4:5]
	v_fma_f32 v185, -v205, v185, v170
	v_cmp_lt_f32_e64 s[4:5], 0, v185
	s_nop 1
	v_cndmask_b32_e64 v185, v204, v205, s[4:5]
	v_mul_f32_e32 v204, 0x37800000, v185
	v_cndmask_b32_e32 v185, v185, v204, vcc
	v_cmp_class_f32_e32 vcc, v170, v196
	s_nop 1
	v_cndmask_b32_e32 v170, v185, v170, vcc
	v_div_scale_f32 v185, s[4:5], v170, v170, v200
	v_rcp_f32_e32 v204, v185
	s_nop 0
	v_fma_f32 v205, -v185, v204, 1.0
	v_fmac_f32_e32 v204, v205, v204
	v_div_scale_f32 v205, vcc, v200, v170, v200
	v_mul_f32_e32 v206, v205, v204
	v_fma_f32 v207, -v185, v206, v205
	v_fmac_f32_e32 v206, v207, v204
	v_fma_f32 v185, -v185, v206, v205
	v_div_fmas_f32 v185, v185, v204, v206
	v_div_fixup_f32 v170, v185, v170, v200
	v_pk_mul_f32 v[212:213], v[14:15], v[170:171] op_sel_hi:[1,0]
	v_pk_mul_f32 v[214:215], v[16:17], v[170:171] op_sel_hi:[1,0]
	v_pk_mul_f32 v[216:217], v[10:11], v[170:171] op_sel_hi:[1,0]
	v_pk_mul_f32 v[218:219], v[12:13], v[170:171] op_sel_hi:[1,0]
	v_pk_mul_f32 v[204:205], v[40:41], v[170:171] op_sel_hi:[1,0]
	v_pk_mul_f32 v[206:207], v[38:39], v[170:171] op_sel_hi:[1,0]
	v_pk_mul_f32 v[208:209], v[36:37], v[170:171] op_sel_hi:[1,0]
	v_pk_mul_f32 v[210:211], v[34:35], v[170:171] op_sel_hi:[1,0]
	v_pk_mul_f32 v[214:215], v[136:137], v[214:215]
	v_pk_mul_f32 v[212:213], v[134:135], v[212:213]
	v_pk_mul_f32 v[218:219], v[132:133], v[218:219]
	v_pk_mul_f32 v[216:217], v[130:131], v[216:217]
	v_pk_mul_f32 v[206:207], v[142:143], v[206:207]
	v_pk_mul_f32 v[204:205], v[144:145], v[204:205]
	v_pk_mul_f32 v[210:211], v[138:139], v[210:211]
	v_pk_mul_f32 v[208:209], v[140:141], v[208:209]
	s_waitcnt lgkmcnt(0)
	v_pk_mul_f32 v[220:221], v[158:159], v[212:213]
	v_pk_mul_f32 v[222:223], v[160:161], v[214:215]
	v_pk_mul_f32 v[224:225], v[150:151], v[216:217]
	v_pk_mul_f32 v[226:227], v[152:153], v[218:219]
	v_pk_fma_f32 v[222:223], v[156:157], v[204:205], v[222:223] neg_lo:[0,0,1] neg_hi:[0,0,1]
	v_pk_fma_f32 v[220:221], v[154:155], v[206:207], v[220:221] neg_lo:[0,0,1] neg_hi:[0,0,1]
	v_pk_fma_f32 v[226:227], v[148:149], v[208:209], v[226:227] neg_lo:[0,0,1] neg_hi:[0,0,1]
	v_pk_fma_f32 v[224:225], v[146:147], v[210:211], v[224:225] neg_lo:[0,0,1] neg_hi:[0,0,1]
	v_pk_mul_f32 v[154:155], v[154:155], v[212:213]
	v_pk_mul_f32 v[156:157], v[156:157], v[214:215]
	v_pk_mul_f32 v[146:147], v[146:147], v[216:217]
	v_pk_mul_f32 v[148:149], v[148:149], v[218:219]
	v_ashrrev_i32_e32 v185, 31, v184
	v_pk_fma_f32 v[156:157], v[160:161], v[204:205], v[156:157]
	v_pk_fma_f32 v[154:155], v[158:159], v[206:207], v[154:155]
	v_pk_fma_f32 v[158:159], v[152:153], v[208:209], v[148:149]
	v_pk_fma_f32 v[152:153], v[150:151], v[210:211], v[146:147]
	v_lshl_add_u64 v[160:161], v[184:185], 1, s[6:7]
	v_cvt_pk_f16_f32 v146, v220, v221
	v_cvt_pk_f16_f32 v147, v222, v223
	v_cvt_pk_f16_f32 v148, v224, v225
	v_cvt_pk_f16_f32 v149, v226, v227
	v_cvt_pk_f16_f32 v150, v154, v155
	v_cvt_pk_f16_f32 v151, v156, v157
	v_cvt_pk_f16_f32 v152, v152, v153
	v_cvt_pk_f16_f32 v153, v158, v159
	global_store_dwordx4 v[160:161], v[146:149], off sc1
	v_add_u32_e32 v208, 0xb0, v199
	v_and_b32_e32 v209, 0x7ff, v208
	v_lshl_add_u64 v[146:147], v[160:161], 0, s[10:11]
	global_store_dwordx4 v[146:147], v[150:153], off sc1
	v_mul_f32_e32 v146, v23, v23
	v_mul_f32_e32 v147, v25, v25
	v_fmac_f32_e32 v146, v22, v22
	v_fmac_f32_e32 v147, v24, v24
	v_add_f32_e32 v152, v146, v147
	v_pk_mul_f32 v[146:147], v[20:21], v[20:21]
	v_pk_mul_f32 v[148:149], v[18:19], v[18:19]
	v_mov_b32_e32 v150, v146
	v_mov_b32_e32 v151, v148
	v_mov_b32_e32 v148, v147
	v_pk_add_f32 v[146:147], v[150:151], v[148:149]
	v_lshlrev_b32_e32 v170, 7, v209
	v_add_f32_e32 v147, v152, v147
	v_add_f32_e32 v210, v146, v147
	ds_read_b128 v[146:149], v245 offset:52224
	s_nop 0
	ds_read_b128 v[150:153], v244 offset:52224
	s_nop 0
	ds_read_b128 v[154:157], v245 offset:19456
	s_nop 0
	ds_read_b128 v[158:161], v244 offset:19456
	v_pk_mul_f32 v[184:185], v[8:9], v[8:9]
	v_pk_mul_f32 v[204:205], v[6:7], v[6:7]
	v_mov_b32_e32 v206, v184
	v_mov_b32_e32 v207, v204
	v_mov_b32_e32 v204, v185
	v_pk_add_f32 v[184:185], v[206:207], v[204:205]
	v_pk_mul_f32 v[204:205], v[2:3], v[2:3]
	v_add_f32_e32 v170, v210, v185
	v_add_f32_e32 v170, v184, v170
	v_pk_mul_f32 v[184:185], v[4:5], v[4:5]
	v_mov_b32_e32 v207, v204
	v_mov_b32_e32 v206, v184
	v_mov_b32_e32 v204, v185
	v_pk_add_f32 v[184:185], v[206:207], v[204:205]
	s_nop 0
	v_add_f32_e32 v170, v185, v170
	v_add_f32_e32 v170, v184, v170
	ds_bpermute_b32 v184, v201, v170
	s_waitcnt lgkmcnt(0)
	v_add_f32_e32 v170, v170, v184
	ds_bpermute_b32 v184, v202, v170
	s_waitcnt lgkmcnt(0)
	v_add_f32_e32 v170, v170, v184
	v_fmamk_f32 v170, v170, 0x3c800000, v195
	v_mul_f32_e32 v184, 0x4f800000, v170
	v_cmp_gt_f32_e32 vcc, s70, v170
	s_nop 1
	v_cndmask_b32_e32 v170, v170, v184, vcc
	v_sqrt_f32_e32 v184, v170
	s_nop 0
	v_add_u32_e32 v185, -1, v184
	v_fma_f32 v201, -v185, v184, v170
	v_cmp_ge_f32_e64 s[4:5], 0, v201
	v_add_u32_e32 v201, 1, v184
	s_nop 0
	v_cndmask_b32_e64 v185, v184, v185, s[4:5]
	v_fma_f32 v184, -v201, v184, v170
	v_cmp_lt_f32_e64 s[4:5], 0, v184
	s_nop 1
	v_cndmask_b32_e64 v184, v185, v201, s[4:5]
	v_mul_f32_e32 v185, 0x37800000, v184
	v_cndmask_b32_e32 v184, v184, v185, vcc
	v_cmp_class_f32_e32 vcc, v170, v196
	s_nop 1
	v_cndmask_b32_e32 v170, v184, v170, vcc
	v_div_scale_f32 v184, s[4:5], v170, v170, v200
	v_rcp_f32_e32 v185, v184
	s_nop 0
	v_fma_f32 v201, -v184, v185, 1.0
	v_fmac_f32_e32 v185, v201, v185
	v_div_scale_f32 v201, vcc, v200, v170, v200
	v_mul_f32_e32 v202, v201, v185
	v_fma_f32 v204, -v184, v202, v201
	v_fmac_f32_e32 v202, v204, v185
	v_fma_f32 v184, -v184, v202, v201
	v_div_fmas_f32 v184, v184, v185, v202
	v_div_fixup_f32 v170, v184, v170, v200
	v_pk_mul_f32 v[184:185], v[24:25], v[170:171] op_sel_hi:[1,0]
	v_pk_mul_f32 v[200:201], v[22:23], v[170:171] op_sel_hi:[1,0]
	v_pk_mul_f32 v[144:145], v[144:145], v[184:185]
	v_pk_mul_f32 v[184:185], v[20:21], v[170:171] op_sel_hi:[1,0]
	v_pk_mul_f32 v[142:143], v[142:143], v[200:201]
	v_pk_mul_f32 v[140:141], v[140:141], v[184:185]
	v_pk_mul_f32 v[184:185], v[6:7], v[170:171] op_sel_hi:[1,0]
	v_pk_mul_f32 v[200:201], v[18:19], v[170:171] op_sel_hi:[1,0]
	v_pk_mul_f32 v[134:135], v[134:135], v[184:185]
	v_pk_mul_f32 v[184:185], v[2:3], v[170:171] op_sel_hi:[1,0]
	v_pk_mul_f32 v[138:139], v[138:139], v[200:201]
	v_pk_mul_f32 v[130:131], v[130:131], v[184:185]
	v_pk_mul_f32 v[200:201], v[8:9], v[170:171] op_sel_hi:[1,0]
	s_waitcnt lgkmcnt(0)
	v_pk_mul_f32 v[204:205], v[146:147], v[130:131]
	s_waitcnt lgkmcnt(0)
	v_pk_mul_f32 v[130:131], v[154:155], v[130:131]
	v_pk_mul_f32 v[136:137], v[136:137], v[200:201]
	v_pk_mul_f32 v[200:201], v[4:5], v[170:171] op_sel_hi:[1,0]
	v_pk_fma_f32 v[204:205], v[154:155], v[138:139], v[204:205] neg_lo:[0,0,1] neg_hi:[0,0,1]
	v_pk_fma_f32 v[138:139], v[146:147], v[138:139], v[130:131]
	v_lshlrev_b32_e32 v130, 6, v209
	v_lshlrev_b32_e32 v131, 3, v208
	v_pk_mul_f32 v[132:133], v[132:133], v[200:201]
	v_and_b32_e32 v130, s37, v130
	v_and_b32_e32 v131, s9, v131
	v_pk_mul_f32 v[184:185], v[150:151], v[134:135]
	v_pk_mul_f32 v[200:201], v[152:153], v[136:137]
	v_pk_mul_f32 v[206:207], v[148:149], v[132:133]
	v_or3_b32 v130, v131, v203, v130
	s_waitcnt lgkmcnt(0)
	v_pk_fma_f32 v[200:201], v[160:161], v[144:145], v[200:201] neg_lo:[0,0,1] neg_hi:[0,0,1]
	v_pk_fma_f32 v[184:185], v[158:159], v[142:143], v[184:185] neg_lo:[0,0,1] neg_hi:[0,0,1]
	v_pk_fma_f32 v[206:207], v[156:157], v[140:141], v[206:207] neg_lo:[0,0,1] neg_hi:[0,0,1]
	v_pk_mul_f32 v[134:135], v[158:159], v[134:135]
	v_pk_mul_f32 v[136:137], v[160:161], v[136:137]
	v_pk_mul_f32 v[132:133], v[156:157], v[132:133]
	v_ashrrev_i32_e32 v131, 31, v130
	v_pk_fma_f32 v[136:137], v[152:153], v[144:145], v[136:137]
	v_pk_fma_f32 v[134:135], v[150:151], v[142:143], v[134:135]
	v_pk_fma_f32 v[140:141], v[148:149], v[140:141], v[132:133]
	v_lshl_add_u64 v[142:143], v[130:131], 1, s[6:7]
	v_cvt_pk_f16_f32 v130, v184, v185
	v_cvt_pk_f16_f32 v131, v200, v201
	v_cvt_pk_f16_f32 v132, v204, v205
	v_cvt_pk_f16_f32 v133, v206, v207
	v_cvt_pk_f16_f32 v134, v134, v135
	v_cvt_pk_f16_f32 v135, v136, v137
	v_cvt_pk_f16_f32 v136, v138, v139
	v_cvt_pk_f16_f32 v137, v140, v141
	global_store_dwordx4 v[142:143], v[130:133], off sc1
	s_nop 1
	v_lshl_add_u64 v[130:131], v[142:143], 0, s[10:11]
	global_store_dwordx4 v[130:131], v[134:137], off sc1
	s_cmp_lg_u32 s94, 0
	s_cbranch_scc1 .LBB1_14
	s_mov_b32 s94, 1
	s_waitcnt vmcnt(0) lgkmcnt(0)
	s_barrier
	s_branch .LBB1_15

	.amdhsa_kernel _Z15gemm_qkv_kernelPKDF16_S0_PDF16_S1_S1_PKfS3_S3_S3_S3_S1_PKiPyPj
		.amdhsa_group_segment_fixed_size 0
		.amdhsa_private_segment_fixed_size 0
		.amdhsa_kernarg_size 112
		.amdhsa_user_sgpr_count 2
		.amdhsa_user_sgpr_dispatch_ptr 0
		.amdhsa_user_sgpr_queue_ptr 0
		.amdhsa_user_sgpr_kernarg_segment_ptr 1
		.amdhsa_user_sgpr_dispatch_id 0
		.amdhsa_user_sgpr_kernarg_preload_length 0
		.amdhsa_user_sgpr_kernarg_preload_offset 0
		.amdhsa_user_sgpr_private_segment_size 0
		.amdhsa_uses_dynamic_stack 0
		.amdhsa_enable_private_segment 0
		.amdhsa_system_sgpr_workgroup_id_x 1
		.amdhsa_system_sgpr_workgroup_id_y 0
		.amdhsa_system_sgpr_workgroup_id_z 0
		.amdhsa_system_sgpr_workgroup_info 0
		.amdhsa_system_vgpr_workitem_id 0
		.amdhsa_next_free_vgpr 248
		.amdhsa_next_free_sgpr 95
		.amdhsa_accum_offset 248
		.amdhsa_reserve_vcc 1
		.amdhsa_float_round_mode_32 0
		.amdhsa_float_round_mode_16_64 0
		.amdhsa_float_denorm_mode_32 3
		.amdhsa_float_denorm_mode_16_64 3
		.amdhsa_dx10_clamp 1
		.amdhsa_ieee_mode 1
		.amdhsa_fp16_overflow 0
		.amdhsa_tg_split 0
		.amdhsa_exception_fp_ieee_invalid_op 0
		.amdhsa_exception_fp_denorm_src 0
		.amdhsa_exception_fp_ieee_div_zero 0
		.amdhsa_exception_fp_ieee_overflow 0
		.amdhsa_exception_fp_ieee_underflow 0
		.amdhsa_exception_fp_ieee_inexact 0
		.amdhsa_exception_int_div_zero 0
	.end_amdhsa_kernel

amdhsa.kernels:
  - .agpr_count:     0
    .args:
      - .actual_access:  read_only
        .address_space:  global
        .offset:         0
        .size:           8
        .value_kind:     global_buffer
      - .actual_access:  read_only
        .address_space:  global
        .offset:         8
        .size:           8
        .value_kind:     global_buffer
      - .actual_access:  read_only
        .address_space:  global
        .offset:         16
        .size:           8
        .value_kind:     global_buffer
      - .actual_access:  write_only
        .address_space:  global
        .offset:         24
        .size:           8
        .value_kind:     global_buffer
      - .actual_access:  write_only
        .address_space:  global
        .offset:         32
        .size:           8
        .value_kind:     global_buffer
      - .actual_access:  write_only
        .address_space:  global
        .offset:         40
        .size:           8
        .value_kind:     global_buffer
      - .actual_access:  write_only
        .address_space:  global
        .offset:         48
        .size:           8
        .value_kind:     global_buffer
    .group_segment_fixed_size: 0
    .kernarg_segment_align: 8
    .kernarg_segment_size: 56
    .language:       OpenCL C
    .language_version:
      - 2
      - 0
    .max_flat_workgroup_size: 1024
    .name:           _Z11prep_kernelPKfS0_PKiPDF16_S3_PfS4_
    .private_segment_fixed_size: 0
    .sgpr_count:     24
    .sgpr_spill_count: 0
    .symbol:         _Z11prep_kernelPKfS0_PKiPDF16_S3_PfS4_.kd
    .uniform_work_group_size: 1
    .uses_dynamic_stack: false
    .vgpr_count:     40
    .vgpr_spill_count: 0
    .wavefront_size: 64
  - .agpr_count:     0
    .args:
      - .address_space:  global
        .offset:         0
        .size:           8
        .value_kind:     global_buffer
      - .address_space:  global
        .offset:         8
        .size:           8
        .value_kind:     global_buffer
      - .address_space:  global
        .offset:         16
        .size:           8
        .value_kind:     global_buffer
      - .address_space:  global
        .offset:         24
        .size:           8
        .value_kind:     global_buffer
      - .address_space:  global
        .offset:         32
        .size:           8
        .value_kind:     global_buffer
      - .address_space:  global
        .offset:         40
        .size:           8
        .value_kind:     global_buffer
      - .address_space:  global
        .offset:         48
        .size:           8
        .value_kind:     global_buffer
      - .address_space:  global
        .offset:         56
        .size:           8
        .value_kind:     global_buffer
      - .address_space:  global
        .offset:         64
        .size:           8
        .value_kind:     global_buffer
      - .address_space:  global
        .offset:         72
        .size:           8
        .value_kind:     global_buffer
      - .address_space:  global
        .offset:         80
        .size:           8
        .value_kind:     global_buffer
      - .address_space:  global
        .offset:         88
        .size:           8
        .value_kind:     global_buffer
      - .address_space:  global
        .offset:         96
        .size:           8
        .value_kind:     global_buffer
      - .address_space:  global
        .offset:         104
        .size:           8
        .value_kind:     global_buffer
    .group_segment_fixed_size: 0
    .kernarg_segment_align: 8
    .kernarg_segment_size: 112
    .language:       OpenCL C
    .language_version:
      - 2
      - 0
    .max_flat_workgroup_size: 512
    .name:           _Z15gemm_qkv_kernelPKDF16_S0_PDF16_S1_S1_PKfS3_S3_S3_S3_S1_PKiPyPj
    .private_segment_fixed_size: 0
    .sgpr_count:     101
    .sgpr_spill_count: 0
    .symbol:         _Z15gemm_qkv_kernelPKDF16_S0_PDF16_S1_S1_PKfS3_S3_S3_S3_S1_PKiPyPj.kd
    .uniform_work_group_size: 1
    .uses_dynamic_stack: false
    .vgpr_count:     248
    .vgpr_spill_count: 0
    .wavefront_size: 64
  - .agpr_count:     0
    .args:
      - .address_space:  global
        .offset:         0
        .size:           8
        .value_kind:     global_buffer
      - .address_space:  global
        .offset:         8
        .size:           8
        .value_kind:     global_buffer
      - .address_space:  global
        .offset:         16
        .size:           8
        .value_kind:     global_buffer
    .group_segment_fixed_size: 0
    .kernarg_segment_align: 8
    .kernarg_segment_size: 24
    .language:       OpenCL C
    .language_version:
      - 2
      - 0
    .max_flat_workgroup_size: 512
    .name:           _Z15gemm_out_kernelPKDF16_S0_Pf
    .private_segment_fixed_size: 0
    .sgpr_count:     26
    .sgpr_spill_count: 0
    .symbol:         _Z15gemm_out_kernelPKDF16_S0_Pf.kd
    .uniform_work_group_size: 1
    .uses_dynamic_stack: false
    .vgpr_count:     148
    .vgpr_spill_count: 0
    .wavefront_size: 64
  - .agpr_count:     0
    .args:
      - .address_space:  global
        .offset:         0
        .size:           8
        .value_kind:     global_buffer
      - .address_space:  global
        .offset:         8
        .size:           8
        .value_kind:     global_buffer
      - .address_space:  global
        .offset:         16
        .size:           8
        .value_kind:     global_buffer
      - .address_space:  global
        .offset:         24
        .size:           8
        .value_kind:     global_buffer
      - .address_space:  global
        .offset:         32
        .size:           8
        .value_kind:     global_buffer
      - .address_space:  global
        .offset:         40
        .size:           8
        .value_kind:     global_buffer
    .group_segment_fixed_size: 0
    .kernarg_segment_align: 8
    .kernarg_segment_size: 48
    .language:       OpenCL C
    .language_version:
      - 2
      - 0
    .max_flat_workgroup_size: 512
    .name:           _Z11attn_kernelPKDF16_S0_S0_PDF16_PKjS3_
    .private_segment_fixed_size: 0
    .sgpr_count:     68
    .sgpr_spill_count: 0
    .symbol:         _Z11attn_kernelPKDF16_S0_S0_PDF16_PKjS3_.kd
    .uniform_work_group_size: 1
    .uses_dynamic_stack: false
    .vgpr_count:     248
    .vgpr_spill_count: 0
    .wavefront_size: 64
